# L0 MLA loop: waves 0-3 s_sleep 2 after each in-loop barrier (stagger attempt) on top of static prio
# baseline (speedup 1.0000x reference)
.Lnoprio_a0:
	s_lshr_b32 s98, s81, 8
	s_mov_b32 s46, s15
	s_mov_b64 s[6:7], s[34:35]
	s_mov_b32 s41, s14
	s_add_i32 s0, 0, 0x20468
	s_add_u32 s8, s6, 0x58000
	v_mov_b32_e32 v0, s0
	s_addc_u32 s9, s7, 0
	s_add_i32 s0, 0, 0x204a0
	s_waitcnt lgkmcnt(0)
	v_mov_b32_e32 v2, s0
	s_add_i32 s0, 0, 0x20488
	s_waitcnt vmcnt(0)
	v_mov_b32_e32 v4, s0
	ds_read_b64 v[0:1], v0
	ds_read_b64 v[2:3], v2
	ds_read_b64 v[4:5], v4
	v_readfirstlane_b32 s47, v184
	s_cmpk_lt_i32 s41, 0x110
	s_cselect_b64 s[12:13], -1, 0
	s_and_b32 s0, s47, 0xffffffc0
	s_mov_b32 s16, 0
	s_waitcnt lgkmcnt(2)
	v_readfirstlane_b32 s10, v0
	v_readfirstlane_b32 s11, v1
	s_waitcnt lgkmcnt(1)
	v_readfirstlane_b32 s48, v2
	v_readfirstlane_b32 s49, v3
	s_waitcnt lgkmcnt(0)
	v_readfirstlane_b32 s38, v4
	v_readfirstlane_b32 s39, v5
	s_cmpk_gt_i32 s41, 0x10f
	v_add_u32_e32 v200, s0, v193
	s_cbranch_scc1 .LBB0_598
	s_add_u32 s50, s6, 0x4619c000
	s_addc_u32 s51, s7, 0
	s_add_u32 s52, s6, 0x49d1c000
	s_addc_u32 s53, s7, 0
	s_add_u32 s54, s6, 0x216b8000
	s_addc_u32 s55, s7, 0
	s_add_u32 s56, s6, 0x37e0c000
	s_addc_u32 s57, s7, 0
	s_movk_i32 s58, 0xff
	s_movk_i32 s59, 0x100
	s_movk_i32 s60, 0x2000
	s_movk_i32 s61, 0xc00
	v_mov_b32_e32 v187, 0
	v_mov_b32_e32 v185, 0x358637bd
	s_mov_b32 s62, 0x800000
	s_mov_b32 s63, 0x2aaaaaab
	s_movk_i32 s64, 0x600
	s_movk_i32 s65, 0xd0
	s_movk_i32 s66, 0x50
	s_add_i32 s67, 0, 0x10000
	s_mov_b32 s68, 0xaaaaaaab
	s_mov_b32 s69, 0xc3e00000
	v_mov_b32_e32 v201, 0x7149f2ca
	s_mov_b32 s40, 0x3dd53b94
	s_mov_b32 s70, 0x41000000
	v_mov_b32_e32 v202, 0xc0a00000
	v_mov_b32_e32 v203, 0x43e00000
	v_mov_b32_e32 v204, 0xf149f2ca
	s_mov_b32 s71, s41
	s_branch .LBB0_548

.LBB0_565:
	s_waitcnt lgkmcnt(4)
	v_mfma_scale_f32_32x32x64_f8f6f4 v[96:111], v[96:103], v[120:127], 0, v205, v205 op_sel_hi:[0,0,0]
	v_cndmask_b32_e64 v176, v189, v192, s[4:5]
	v_fma_f32 v80, v80, s40, -v176
	v_fma_f32 v81, v81, s40, -v176
	v_fma_f32 v84, v84, s40, -v176
	v_fma_f32 v85, v85, s40, -v176
	v_fma_f32 v88, v88, s40, -v176
	v_fma_f32 v89, v89, s40, -v176
	v_fma_f32 v92, v92, s40, -v176
	v_fma_f32 v93, v93, s40, -v176
	v_exp_f32_e32 v80, v80
	v_exp_f32_e32 v81, v81
	v_exp_f32_e32 v84, v84
	v_exp_f32_e32 v85, v85
	v_exp_f32_e32 v88, v88
	v_exp_f32_e32 v89, v89
	s_waitcnt lgkmcnt(2)
	v_mfma_scale_f32_32x32x64_f8f6f4 v[96:111], v[156:163], v[128:135], v[96:111], v205, v205 op_sel_hi:[0,0,0]
	v_exp_f32_e32 v92, v92
	v_exp_f32_e32 v93, v93
	v_fma_f32 v82, v82, s40, -v176
	v_fma_f32 v83, v83, s40, -v176
	v_fma_f32 v86, v86, s40, -v176
	v_fma_f32 v87, v87, s40, -v176
	v_fma_f32 v90, v90, s40, -v176
	v_fma_f32 v91, v91, s40, -v176
	v_fma_f32 v94, v94, s40, -v176
	v_fma_f32 v95, v95, s40, -v176
	v_exp_f32_e32 v82, v82
	v_exp_f32_e32 v83, v83
	v_exp_f32_e32 v86, v86
	v_exp_f32_e32 v87, v87
	v_exp_f32_e32 v90, v90
	s_waitcnt lgkmcnt(0)
	v_mfma_scale_f32_32x32x64_f8f6f4 v[96:111], v[148:155], v[136:143], v[96:111], v205, v205 op_sel_hi:[0,0,0]
	v_mov_b32_e32 v148, 0
	v_mov_b32_e32 v149, 0
	v_mov_b32_e32 v150, 0
	v_mov_b32_e32 v151, 0
	v_exp_f32_e32 v91, v91
	v_exp_f32_e32 v94, v94
	v_exp_f32_e32 v95, v95
	v_cvt_pk_fp8_f32 v148, v80, v81
	v_cvt_pk_fp8_f32 v149, v84, v85
	v_cvt_pk_fp8_f32 v150, v88, v89
	v_cvt_pk_fp8_f32 v151, v92, v93
	v_lshl_add_u32 v156, s23, 14, v211
	v_cvt_pk_fp8_f32 v148, v82, v83 op_sel:[0,0,1]
	v_cvt_pk_fp8_f32 v149, v86, v87 op_sel:[0,0,1]
	v_cvt_pk_fp8_f32 v150, v90, v91 op_sel:[0,0,1]
	v_cvt_pk_fp8_f32 v151, v94, v95 op_sel:[0,0,1]
	ds_read_b128 v[80:83], v156
	ds_read_b128 v[84:87], v156 offset:16
	ds_read_b128 v[88:91], v156 offset:2560
	ds_read_b128 v[92:95], v156 offset:2576
	s_waitcnt lgkmcnt(0)
	s_waitcnt lgkmcnt(2)
	v_mfma_scale_f32_32x32x64_f8f6f4 v[48:63], v[144:151], v[80:87], v[48:63], v205, v205 op_sel_hi:[0,0,0]
	ds_read_b128 v[80:83], v156 offset:5120
	ds_read_b128 v[84:87], v156 offset:5136
	ds_read_b128 v[152:155], v156 offset:7680
	ds_read_b128 v[156:159], v156 offset:7696
	s_waitcnt lgkmcnt(0)
	s_waitcnt lgkmcnt(4)
	v_mfma_scale_f32_32x32x64_f8f6f4 v[32:47], v[144:151], v[88:95], v[32:47], v205, v205 op_sel_hi:[0,0,0]
	v_max_f32_e32 v88, v97, v97
	v_max_f32_e32 v89, v96, v96
	v_max_f32_e32 v88, v89, v88
	v_max3_f32 v88, v88, v98, v99
	v_max3_f32 v88, v88, v100, v101
	v_max3_f32 v88, v88, v102, v103
	v_max3_f32 v88, v88, v104, v105
	v_max3_f32 v88, v88, v106, v107
	s_waitcnt lgkmcnt(2)
	v_mfma_scale_f32_32x32x64_f8f6f4 v[16:31], v[144:151], v[80:87], v[16:31], v205, v205 op_sel_hi:[0,0,0]
	v_max3_f32 v88, v88, v108, v109
	v_max3_f32 v88, v88, v110, v111
	v_mov_b32_e32 v89, v88
	s_nop 1
	v_permlane32_swap_b32_e32 v88, v89
	v_max_f32_e32 v80, v89, v89
	v_max_f32_e32 v81, v88, v88
	v_max_f32_e32 v80, v81, v80
	v_fma_f32 v81, v80, s40, -v176
	v_cmp_ge_f32_e32 vcc, s70, v81
	v_fmamk_f32 v80, v80, 0x3dd53b94, v202
	v_max_f32_e32 v81, v176, v176
	v_max_f32_e32 v80, v81, v80
	v_sub_f32_e32 v81, v176, v80
	v_exp_f32_e32 v81, v81
	s_waitcnt lgkmcnt(0)
	v_mfma_scale_f32_32x32x64_f8f6f4 v[0:15], v[144:151], v[152:159], v[0:15], v205, v205 op_sel_hi:[0,0,0]
	s_cmp_eq_u64 vcc, exec
	s_cselect_b64 vcc, -1, 0
	v_cndmask_b32_e32 v192, v80, v176, vcc
	s_add_i32 s21, s21, 2
	s_add_i32 s78, s78, 1
	s_add_i32 s22, s22, 64
	v_fma_f32 v178, v96, s40, -v192
	v_fma_f32 v179, v97, s40, -v192
	v_fma_f32 v176, v98, s40, -v192
	v_fma_f32 v177, v99, s40, -v192
	v_fma_f32 v162, v100, s40, -v192
	v_fma_f32 v163, v101, s40, -v192
	v_fma_f32 v160, v102, s40, -v192
	v_fma_f32 v161, v103, s40, -v192
	v_pk_fma_f32 v[158:159], v[104:105], s[40:41], v[192:193] op_sel_hi:[1,0,0] neg_lo:[0,0,1] neg_hi:[0,0,1]
	v_pk_fma_f32 v[156:157], v[106:107], s[40:41], v[192:193] op_sel_hi:[1,0,0] neg_lo:[0,0,1] neg_hi:[0,0,1]
	v_pk_fma_f32 v[154:155], v[108:109], s[40:41], v[192:193] op_sel_hi:[1,0,0] neg_lo:[0,0,1] neg_hi:[0,0,1]
	v_pk_fma_f32 v[152:153], v[110:111], s[40:41], v[192:193] op_sel_hi:[1,0,0] neg_lo:[0,0,1] neg_hi:[0,0,1]
	v_cndmask_b32_e64 v88, v81, 1.0, vcc
	v_mfma_scale_f32_32x32x64_f8f6f4 v[64:79], v[144:151], v[112:119], v[64:79], v205, v205 op_sel_hi:[0,0,0]
	s_cmp_ge_u32 s21, s17
	s_barrier
	s_cselect_b32 s100, 1, 0
	s_cmp_eq_u32 s98, 0
	s_cbranch_scc0 .Lstg_a0
	s_sleep 2
.Lstg_a0:
	s_cmp_lg_u32 s100, 0
	s_cbranch_scc1 .LBB0_580

.LBB0_577:
	v_mul_f32_e32 v96, 0x3dd53b94, v96
	v_add_f32_e32 v96, 0xc0a00000, v96
	v_max_f32_e32 v97, v192, v192
	v_max_f32_e32 v189, v97, v96
	v_sub_f32_e32 v96, v192, v189
	v_exp_f32_e32 v96, v96
	s_cmp_eq_u64 vcc, s[4:5]
	s_cselect_b64 s[4:5], -1, 0
	v_exp_f32_e32 v97, v179
	v_cndmask_b32_e64 v191, v96, 1.0, s[4:5]
	v_exp_f32_e32 v96, v178
	v_exp_f32_e32 v100, v162
	v_exp_f32_e32 v101, v163
	v_exp_f32_e32 v104, v158
	v_exp_f32_e32 v105, v159
	v_exp_f32_e32 v108, v154
	v_exp_f32_e32 v109, v155
	v_mov_b32_e32 v144, 0
	v_mov_b32_e32 v145, 0
	v_exp_f32_e32 v98, v176
	v_exp_f32_e32 v99, v177
	v_exp_f32_e32 v102, v160
	v_exp_f32_e32 v103, v161
	v_cvt_pk_fp8_f32 v144, v96, v97
	v_cvt_pk_fp8_f32 v145, v100, v101
	v_mov_b32_e32 v146, 0
	v_mov_b32_e32 v147, 0
	s_xor_b32 s18, s24, 0x8000
	v_exp_f32_e32 v106, v156
	v_exp_f32_e32 v107, v157
	v_exp_f32_e32 v110, v152
	v_cvt_pk_fp8_f32 v146, v104, v105
	v_exp_f32_e32 v104, v153
	v_cvt_pk_fp8_f32 v147, v108, v109
	v_add_u32_e32 v105, s18, v216
	v_cvt_pk_fp8_f32 v144, v98, v99 op_sel:[0,0,1]
	v_cvt_pk_fp8_f32 v145, v102, v103 op_sel:[0,0,1]
	s_waitcnt lgkmcnt(0)
	s_barrier
	s_cmp_eq_u32 s98, 0
	s_cbranch_scc0 .Lstg_b0
	s_sleep 2
.Lstg_b0:
	ds_read_b128 v[96:99], v105
	ds_read_b128 v[100:103], v105 offset:16
	ds_read_b128 v[156:159], v105 offset:64
	ds_read_b128 v[160:163], v105 offset:80
	v_add_u32_e32 v105, v105, v217
	ds_read_b128 v[148:151], v105 offset:128
	ds_read_b128 v[152:155], v105 offset:160
	v_cvt_pk_fp8_f32 v146, v106, v107 op_sel:[0,0,1]
	v_cvt_pk_fp8_f32 v147, v110, v104 op_sel:[0,0,1]
	v_cmp_gt_f32_e32 vcc, 1.0, v191
	s_cbranch_vccz .LBB0_565
	s_and_saveexec_b64 s[18:19], s[2:3]
	s_cbranch_execz .LBB0_564
	ds_write_b32 v209, v191 offset:128
	s_branch .LBB0_564
